# converter W1 items re-shaped: each reads 128 k-rows x 1 KiB contiguous (256 columns of the glu or lin half) and writes two 128-row output tiles, instead of two 512-byte segments per row
# speedup vs baseline: 1.0309x; 1.0063x over previous
.LBB0_226:
	s_cmp_lt_i32 s28, 3
	s_cselect_b64 s[0:1], -1, 0
	s_cmp_gt_i32 s29, 2
	s_cselect_b64 s[6:7], -1, 0
	s_and_b64 s[0:1], s[0:1], s[6:7]
	s_andn2_b64 vcc, exec, s[0:1]
	s_cbranch_vccnz .LBB0_398
	s_cmpk_lg_i32 s33, 0x100
	s_cselect_b32 s3, s33, 0x78
	s_sub_i32 s6, s33, s3
	s_cmp_lt_i32 s2, s6
	s_cselect_b64 s[0:1], -1, 0
	s_sub_i32 s30, s2, s6
	s_cmpk_gt_i32 s30, 0x2fff
	s_cselect_b64 s[6:7], -1, 0
	s_or_b64 s[0:1], s[0:1], s[6:7]
	v_lshrrev_b32_e32 v82, 5, v0
	v_lshlrev_b32_e32 v80, 4, v0
	v_lshrrev_b32_e32 v1, 7, v0
	v_lshrrev_b32_e32 v81, 3, v0
	s_and_b64 vcc, exec, s[0:1]
	s_cbranch_vccnz .LBB0_237
	v_readlane_b32 s6, v252, 0
	v_readlane_b32 s7, v252, 1
	v_readfirstlane_b32 s34, v0
	s_nop 4
	s_sub_u32 s6, s6, 0xe8
	s_subb_u32 s7, s7, 0
	s_load_dwordx2 s[8:9], s[6:7], 0xa8
	s_load_dwordx2 s[10:11], s[6:7], 0xb8
	s_lshr_b32 s34, s34, 6
	s_add_u32 s12, s26, 0x5800000
	s_addc_u32 s13, s27, 0
	s_add_u32 s14, s26, 0x25800000
	s_addc_u32 s15, s27, 0
	s_mov_b32 s35, 0xc3e00000
	v_mov_b32_e32 v160, 0x43e00000
	s_mov_b32 s31, 120
	s_sub_u32 s0, 0x2fff, s30
	s_mul_hi_u32 s41, s0, 0x2222223
	s_add_u32 s41, s41, 1
	v_and_b32_e32 v77, 63, v0
	v_and_b32_e32 v66, 31, v77
	v_lshlrev_b32_e32 v66, 4, v66
	v_lshrrev_b32_e32 v67, 5, v77
	v_lshlrev_b32_e32 v68, 4, v77
	v_lshl_add_u32 v69, v67, 9, v66
	s_lshr_b32 s0, s34, 1
	v_and_b32_e32 v78, 3, v77
	v_xor_b32_e32 v78, s0, v78
	v_and_b32_e32 v71, 4, v77
	v_or_b32_e32 v78, v78, v71
	v_lshlrev_b32_e32 v78, 4, v78
	s_and_b32 s0, s34, 1
	s_lshl_b32 s0, s0, 3
	v_lshl_or_b32 v71, v77, 9, s0
	v_or_b32_e32 v71, v71, v78
	v_xor_b32_e32 v72, 64, v71
	v_add_u32_e32 v73, 0x8000, v71
	v_add_u32_e32 v74, 0x8000, v72
	s_lshl_b32 s0, s34, 1
	v_add_u32_e32 v78, s0, v67
	v_xor_b32_e32 v78, v78, v77
	v_and_b32_e32 v78, 7, v78
	v_lshlrev_b32_e32 v78, 4, v78
	v_lshrrev_b32_e32 v75, 3, v77
	s_lshl_b32 s0, s34, 3
	v_add_u32_e32 v75, s0, v75
	v_and_b32_e32 v76, 7, v77
	v_lshlrev_b32_e32 v76, 4, v76
	v_lshl_add_u32 v76, v75, 11, v76
	v_lshl_add_u32 v75, v75, 7, v78
	s_waitcnt lgkmcnt(0)
	s_min_u32 s0, s30, 0x2fff
	s_add_u32 s30, s30, s31
	s_cmp_lt_u32 s0, 0x2000
	s_cbranch_scc0 .Lcv_w2_1
	s_lshr_b32 s1, s0, 8
	s_bfe_u32 s3, s0, 0x40004
	s_bfe_u32 s7, s0, 0x30001
	s_and_b32 s0, s0, 1
	s_lshl_b32 s6, s1, 25
	s_lshl_b32 s49, s3, 21
	s_add_u32 s6, s6, s49
	s_lshl_b32 s49, s34, 17
	s_add_u32 s6, s6, s49
	s_lshl_b32 s49, s0, 13
	s_add_u32 s6, s6, s49
	s_lshl_b32 s49, s7, 10
	s_add_u32 s6, s6, s49
	s_add_u32 s62, s8, s6
	s_addc_u32 s63, s9, 0
	s_lshl_b32 s6, s1, 23
	s_lshl_b32 s49, s7, 20
	s_add_u32 s6, s6, s49
	s_lshl_b32 s49, s0, 18
	s_add_u32 s6, s6, s49
	s_lshl_b32 s49, s3, 7
	s_add_u32 s6, s6, s49
	s_add_u32 s52, s12, s6
	s_addc_u32 s53, s13, 0
	s_mov_b32 s70, 0x4000
	s_mov_b32 s71, 0xe4000
	s_mov_b32 s86, 0x60000
	v_mov_b32_e32 v70, v68
	s_branch .Lcv_dec_done_1
.Lcv_w2_1:
	s_sub_u32 s0, s0, 0x2000
	s_lshr_b32 s1, s0, 7
	s_bfe_u32 s3, s0, 0x40003
	s_and_b32 s0, s0, 7
	s_lshl_b32 s6, s1, 24
	s_lshl_b32 s7, s3, 20
	s_add_u32 s6, s6, s7
	s_lshl_b32 s7, s34, 16
	s_add_u32 s6, s6, s7
	s_lshl_b32 s7, s0, 10
	s_add_u32 s6, s6, s7
	s_add_u32 s62, s10, s6
	s_addc_u32 s63, s11, 0
	s_lshl_b32 s6, s1, 22
	s_lshl_b32 s7, s0, 19
	s_add_u32 s6, s6, s7
	s_lshl_b32 s7, s3, 7
	s_add_u32 s6, s6, s7
	s_add_u32 s52, s14, s6
	s_addc_u32 s53, s15, 0
	s_mov_b32 s70, 0x2000
	s_mov_b32 s71, 0x72000
	s_mov_b32 s86, 0x20000
	v_mov_b32_e32 v70, v69
.Lcv_dec_done_1:
	global_load_dwordx4 v[2:5], v70, s[62:63] nt
	s_add_u32 s62, s62, s70
	s_addc_u32 s63, s63, 0
	global_load_dwordx4 v[6:9], v70, s[62:63] nt
	s_add_u32 s62, s62, s70
	s_addc_u32 s63, s63, 0
	global_load_dwordx4 v[10:13], v70, s[62:63] nt
	s_add_u32 s62, s62, s70
	s_addc_u32 s63, s63, 0
	global_load_dwordx4 v[14:17], v70, s[62:63] nt
	s_add_u32 s62, s62, s70
	s_addc_u32 s63, s63, 0
	global_load_dwordx4 v[18:21], v70, s[62:63] nt
	s_add_u32 s62, s62, s70
	s_addc_u32 s63, s63, 0
	global_load_dwordx4 v[22:25], v70, s[62:63] nt
	s_add_u32 s62, s62, s70
	s_addc_u32 s63, s63, 0
	global_load_dwordx4 v[26:29], v70, s[62:63] nt
	s_add_u32 s62, s62, s70
	s_addc_u32 s63, s63, 0
	global_load_dwordx4 v[30:33], v70, s[62:63] nt
	s_add_u32 s62, s62, s71
	s_addc_u32 s63, s63, 0
	global_load_dwordx4 v[34:37], v70, s[62:63] nt
	s_add_u32 s62, s62, s70
	s_addc_u32 s63, s63, 0
	global_load_dwordx4 v[38:41], v70, s[62:63] nt
	s_add_u32 s62, s62, s70
	s_addc_u32 s63, s63, 0
	global_load_dwordx4 v[42:45], v70, s[62:63] nt
	s_add_u32 s62, s62, s70
	s_addc_u32 s63, s63, 0
	global_load_dwordx4 v[46:49], v70, s[62:63] nt
	s_add_u32 s62, s62, s70
	s_addc_u32 s63, s63, 0
	global_load_dwordx4 v[50:53], v70, s[62:63] nt
	s_add_u32 s62, s62, s70
	s_addc_u32 s63, s63, 0
	global_load_dwordx4 v[54:57], v70, s[62:63] nt
	s_add_u32 s62, s62, s70
	s_addc_u32 s63, s63, 0
	global_load_dwordx4 v[58:61], v70, s[62:63] nt
	s_add_u32 s62, s62, s70
	s_addc_u32 s63, s63, 0
	global_load_dwordx4 v[62:65], v70, s[62:63] nt
	s_min_u32 s0, s30, 0x2fff
	s_add_u32 s30, s30, s31
	s_cmp_lt_u32 s0, 0x2000
	s_cbranch_scc0 .Lcv_w2_2
	s_lshr_b32 s1, s0, 8
	s_bfe_u32 s3, s0, 0x40004
	s_bfe_u32 s7, s0, 0x30001
	s_and_b32 s0, s0, 1
	s_lshl_b32 s6, s1, 25
	s_lshl_b32 s49, s3, 21
	s_add_u32 s6, s6, s49
	s_lshl_b32 s49, s34, 17
	s_add_u32 s6, s6, s49
	s_lshl_b32 s49, s0, 13
	s_add_u32 s6, s6, s49
	s_lshl_b32 s49, s7, 10
	s_add_u32 s6, s6, s49
	s_add_u32 s62, s8, s6
	s_addc_u32 s63, s9, 0
	s_lshl_b32 s6, s1, 23
	s_lshl_b32 s49, s7, 20
	s_add_u32 s6, s6, s49
	s_lshl_b32 s49, s0, 18
	s_add_u32 s6, s6, s49
	s_lshl_b32 s49, s3, 7
	s_add_u32 s6, s6, s49
	s_add_u32 s58, s12, s6
	s_addc_u32 s59, s13, 0
	s_mov_b32 s70, 0x4000
	s_mov_b32 s71, 0xe4000
	s_mov_b32 s87, 0x60000
	v_mov_b32_e32 v70, v68
	s_branch .Lcv_dec_done_2
.Lcv_w2_2:
	s_sub_u32 s0, s0, 0x2000
	s_lshr_b32 s1, s0, 7
	s_bfe_u32 s3, s0, 0x40003
	s_and_b32 s0, s0, 7
	s_lshl_b32 s6, s1, 24
	s_lshl_b32 s7, s3, 20
	s_add_u32 s6, s6, s7
	s_lshl_b32 s7, s34, 16
	s_add_u32 s6, s6, s7
	s_lshl_b32 s7, s0, 10
	s_add_u32 s6, s6, s7
	s_add_u32 s62, s10, s6
	s_addc_u32 s63, s11, 0
	s_lshl_b32 s6, s1, 22
	s_lshl_b32 s7, s0, 19
	s_add_u32 s6, s6, s7
	s_lshl_b32 s7, s3, 7
	s_add_u32 s6, s6, s7
	s_add_u32 s58, s14, s6
	s_addc_u32 s59, s15, 0
	s_mov_b32 s70, 0x2000
	s_mov_b32 s71, 0x72000
	s_mov_b32 s87, 0x20000
	v_mov_b32_e32 v70, v69

.Lcv_convA:
	v_mul_f32_e32 v156, 0x44000000, v2
	v_mul_f32_e32 v157, 0x44000000, v6
	v_med3_f32 v156, v156, s35, v160
	v_med3_f32 v157, v157, s35, v160
	v_cvt_pk_fp8_f32 v148, v156, v157
	v_mul_f32_e32 v158, 0x44000000, v10
	v_mul_f32_e32 v159, 0x44000000, v14
	v_med3_f32 v158, v158, s35, v160
	v_med3_f32 v159, v159, s35, v160
	v_cvt_pk_fp8_f32 v148, v158, v159 op_sel:[0,0,1]
	v_mul_f32_e32 v156, 0x44000000, v18
	v_mul_f32_e32 v157, 0x44000000, v22
	v_med3_f32 v156, v156, s35, v160
	v_med3_f32 v157, v157, s35, v160
	v_cvt_pk_fp8_f32 v149, v156, v157
	v_mul_f32_e32 v158, 0x44000000, v26
	v_mul_f32_e32 v159, 0x44000000, v30
	v_med3_f32 v158, v158, s35, v160
	v_med3_f32 v159, v159, s35, v160
	v_cvt_pk_fp8_f32 v149, v158, v159 op_sel:[0,0,1]
	v_mul_f32_e32 v156, 0x44000000, v3
	v_mul_f32_e32 v157, 0x44000000, v7
	v_med3_f32 v156, v156, s35, v160
	v_med3_f32 v157, v157, s35, v160
	v_cvt_pk_fp8_f32 v150, v156, v157
	v_mul_f32_e32 v158, 0x44000000, v11
	v_mul_f32_e32 v159, 0x44000000, v15
	v_med3_f32 v158, v158, s35, v160
	v_med3_f32 v159, v159, s35, v160
	v_cvt_pk_fp8_f32 v150, v158, v159 op_sel:[0,0,1]
	v_mul_f32_e32 v156, 0x44000000, v19
	v_mul_f32_e32 v157, 0x44000000, v23
	v_med3_f32 v156, v156, s35, v160
	v_med3_f32 v157, v157, s35, v160
	v_cvt_pk_fp8_f32 v151, v156, v157
	v_mul_f32_e32 v158, 0x44000000, v27
	v_mul_f32_e32 v159, 0x44000000, v31
	v_med3_f32 v158, v158, s35, v160
	v_med3_f32 v159, v159, s35, v160
	v_cvt_pk_fp8_f32 v151, v158, v159 op_sel:[0,0,1]
	v_mul_f32_e32 v156, 0x44000000, v4
	v_mul_f32_e32 v157, 0x44000000, v8
	v_med3_f32 v156, v156, s35, v160
	v_med3_f32 v157, v157, s35, v160
	v_cvt_pk_fp8_f32 v152, v156, v157
	v_mul_f32_e32 v158, 0x44000000, v12
	v_mul_f32_e32 v159, 0x44000000, v16
	v_med3_f32 v158, v158, s35, v160
	v_med3_f32 v159, v159, s35, v160
	v_cvt_pk_fp8_f32 v152, v158, v159 op_sel:[0,0,1]
	ds_write2_b64 v71, v[148:149], v[150:151] offset0:0 offset1:16
	v_mul_f32_e32 v156, 0x44000000, v20
	v_mul_f32_e32 v157, 0x44000000, v24
	v_med3_f32 v156, v156, s35, v160
	v_med3_f32 v157, v157, s35, v160
	v_cvt_pk_fp8_f32 v153, v156, v157
	v_mul_f32_e32 v158, 0x44000000, v28
	v_mul_f32_e32 v159, 0x44000000, v32
	v_med3_f32 v158, v158, s35, v160
	v_med3_f32 v159, v159, s35, v160
	v_cvt_pk_fp8_f32 v153, v158, v159 op_sel:[0,0,1]
	v_mul_f32_e32 v156, 0x44000000, v5
	v_mul_f32_e32 v157, 0x44000000, v9
	v_med3_f32 v156, v156, s35, v160
	v_med3_f32 v157, v157, s35, v160
	v_cvt_pk_fp8_f32 v154, v156, v157
	v_mul_f32_e32 v158, 0x44000000, v13
	v_mul_f32_e32 v159, 0x44000000, v17
	v_med3_f32 v158, v158, s35, v160
	v_med3_f32 v159, v159, s35, v160
	v_cvt_pk_fp8_f32 v154, v158, v159 op_sel:[0,0,1]
	v_mul_f32_e32 v156, 0x44000000, v21
	v_mul_f32_e32 v157, 0x44000000, v25
	v_med3_f32 v156, v156, s35, v160
	v_med3_f32 v157, v157, s35, v160
	v_cvt_pk_fp8_f32 v155, v156, v157
	v_mul_f32_e32 v158, 0x44000000, v29
	v_mul_f32_e32 v159, 0x44000000, v33
	v_med3_f32 v158, v158, s35, v160
	v_med3_f32 v159, v159, s35, v160
	v_cvt_pk_fp8_f32 v155, v158, v159 op_sel:[0,0,1]
	v_mul_f32_e32 v156, 0x44000000, v34
	v_mul_f32_e32 v157, 0x44000000, v38
	v_med3_f32 v156, v156, s35, v160
	v_med3_f32 v157, v157, s35, v160
	v_cvt_pk_fp8_f32 v148, v156, v157
	v_mul_f32_e32 v158, 0x44000000, v42
	v_mul_f32_e32 v159, 0x44000000, v46
	v_med3_f32 v158, v158, s35, v160
	v_med3_f32 v159, v159, s35, v160
	v_cvt_pk_fp8_f32 v148, v158, v159 op_sel:[0,0,1]
	ds_write2_b64 v71, v[152:153], v[154:155] offset0:32 offset1:48
	v_mul_f32_e32 v156, 0x44000000, v50
	v_mul_f32_e32 v157, 0x44000000, v54
	v_med3_f32 v156, v156, s35, v160
	v_med3_f32 v157, v157, s35, v160
	v_cvt_pk_fp8_f32 v149, v156, v157
	v_mul_f32_e32 v158, 0x44000000, v58
	v_mul_f32_e32 v159, 0x44000000, v62
	v_med3_f32 v158, v158, s35, v160
	v_med3_f32 v159, v159, s35, v160
	v_cvt_pk_fp8_f32 v149, v158, v159 op_sel:[0,0,1]
	v_mul_f32_e32 v156, 0x44000000, v35
	v_mul_f32_e32 v157, 0x44000000, v39
	v_med3_f32 v156, v156, s35, v160
	v_med3_f32 v157, v157, s35, v160
	v_cvt_pk_fp8_f32 v150, v156, v157
	v_mul_f32_e32 v158, 0x44000000, v43
	v_mul_f32_e32 v159, 0x44000000, v47
	v_med3_f32 v158, v158, s35, v160
	v_med3_f32 v159, v159, s35, v160
	v_cvt_pk_fp8_f32 v150, v158, v159 op_sel:[0,0,1]
	v_mul_f32_e32 v156, 0x44000000, v51
	v_mul_f32_e32 v157, 0x44000000, v55
	v_med3_f32 v156, v156, s35, v160
	v_med3_f32 v157, v157, s35, v160
	v_cvt_pk_fp8_f32 v151, v156, v157
	v_mul_f32_e32 v158, 0x44000000, v59
	v_mul_f32_e32 v159, 0x44000000, v63
	v_med3_f32 v158, v158, s35, v160
	v_med3_f32 v159, v159, s35, v160
	v_cvt_pk_fp8_f32 v151, v158, v159 op_sel:[0,0,1]
	v_mul_f32_e32 v156, 0x44000000, v36
	v_mul_f32_e32 v157, 0x44000000, v40
	v_med3_f32 v156, v156, s35, v160
	v_med3_f32 v157, v157, s35, v160
	v_cvt_pk_fp8_f32 v152, v156, v157
	v_mul_f32_e32 v158, 0x44000000, v44
	v_mul_f32_e32 v159, 0x44000000, v48
	v_med3_f32 v158, v158, s35, v160
	v_med3_f32 v159, v159, s35, v160
	v_cvt_pk_fp8_f32 v152, v158, v159 op_sel:[0,0,1]
	ds_write2_b64 v72, v[148:149], v[150:151] offset0:0 offset1:16
	v_mul_f32_e32 v156, 0x44000000, v52
	v_mul_f32_e32 v157, 0x44000000, v56
	v_med3_f32 v156, v156, s35, v160
	v_med3_f32 v157, v157, s35, v160
	v_cvt_pk_fp8_f32 v153, v156, v157
	v_mul_f32_e32 v158, 0x44000000, v60
	v_mul_f32_e32 v159, 0x44000000, v64
	v_med3_f32 v158, v158, s35, v160
	v_med3_f32 v159, v159, s35, v160
	v_cvt_pk_fp8_f32 v153, v158, v159 op_sel:[0,0,1]
	v_mul_f32_e32 v156, 0x44000000, v37
	v_mul_f32_e32 v157, 0x44000000, v41
	v_med3_f32 v156, v156, s35, v160
	v_med3_f32 v157, v157, s35, v160
	v_cvt_pk_fp8_f32 v154, v156, v157
	v_mul_f32_e32 v158, 0x44000000, v45
	v_mul_f32_e32 v159, 0x44000000, v49
	v_med3_f32 v158, v158, s35, v160
	v_med3_f32 v159, v159, s35, v160
	v_cvt_pk_fp8_f32 v154, v158, v159 op_sel:[0,0,1]
	v_mul_f32_e32 v156, 0x44000000, v53
	v_mul_f32_e32 v157, 0x44000000, v57
	v_med3_f32 v156, v156, s35, v160
	v_med3_f32 v157, v157, s35, v160
	v_cvt_pk_fp8_f32 v155, v156, v157
	v_mul_f32_e32 v158, 0x44000000, v61
	v_mul_f32_e32 v159, 0x44000000, v65
	v_med3_f32 v158, v158, s35, v160
	v_med3_f32 v159, v159, s35, v160
	v_cvt_pk_fp8_f32 v155, v158, v159 op_sel:[0,0,1]
	s_nop 0
	ds_write2_b64 v72, v[152:153], v[154:155] offset0:32 offset1:48
	s_waitcnt lgkmcnt(0)
	s_barrier
	ds_read_b128 v[236:239], v75 offset:0
	ds_read_b128 v[240:243], v75 offset:8192
	ds_read_b128 v[244:247], v75 offset:16384
	ds_read_b128 v[248:251], v75 offset:24576
	s_mov_b64 s[68:69], s[52:53]
	s_waitcnt lgkmcnt(3)
	global_store_dwordx4 v76, v[236:239], s[68:69] nt
	s_add_u32 s68, s68, 0x20000
	s_addc_u32 s69, s69, 0
	s_waitcnt lgkmcnt(2)
	global_store_dwordx4 v76, v[240:243], s[68:69] nt
	s_add_u32 s68, s68, s86
	s_addc_u32 s69, s69, 0
	s_waitcnt lgkmcnt(1)
	global_store_dwordx4 v76, v[244:247], s[68:69] nt
	s_add_u32 s68, s68, 0x20000
	s_addc_u32 s69, s69, 0
	s_waitcnt lgkmcnt(0)
	global_store_dwordx4 v76, v[248:251], s[68:69] nt
	s_sub_u32 s41, s41, 1
	s_cmp_eq_u32 s41, 0
	s_cbranch_scc1 .Lcv_done
	s_min_u32 s0, s30, 0x2fff
	s_add_u32 s30, s30, s31
	s_cmp_lt_u32 s0, 0x2000
	s_cbranch_scc0 .Lcv_w2_3
	s_lshr_b32 s1, s0, 8
	s_bfe_u32 s3, s0, 0x40004
	s_bfe_u32 s7, s0, 0x30001
	s_and_b32 s0, s0, 1
	s_lshl_b32 s6, s1, 25
	s_lshl_b32 s49, s3, 21
	s_add_u32 s6, s6, s49
	s_lshl_b32 s49, s34, 17
	s_add_u32 s6, s6, s49
	s_lshl_b32 s49, s0, 13
	s_add_u32 s6, s6, s49
	s_lshl_b32 s49, s7, 10
	s_add_u32 s6, s6, s49
	s_add_u32 s62, s8, s6
	s_addc_u32 s63, s9, 0
	s_lshl_b32 s6, s1, 23
	s_lshl_b32 s49, s7, 20
	s_add_u32 s6, s6, s49
	s_lshl_b32 s49, s0, 18
	s_add_u32 s6, s6, s49
	s_lshl_b32 s49, s3, 7
	s_add_u32 s6, s6, s49
	s_add_u32 s52, s12, s6
	s_addc_u32 s53, s13, 0
	s_mov_b32 s70, 0x4000
	s_mov_b32 s71, 0xe4000
	s_mov_b32 s86, 0x60000
	v_mov_b32_e32 v70, v68
	s_branch .Lcv_dec_done_3

.Lcv_loopB:
	s_waitcnt vmcnt(20)
	v_mul_f32_e32 v156, 0x44000000, v84
	v_mul_f32_e32 v157, 0x44000000, v88
	v_med3_f32 v156, v156, s35, v160
	v_med3_f32 v157, v157, s35, v160
	v_cvt_pk_fp8_f32 v148, v156, v157
	v_mul_f32_e32 v158, 0x44000000, v92
	v_mul_f32_e32 v159, 0x44000000, v96
	v_med3_f32 v158, v158, s35, v160
	v_med3_f32 v159, v159, s35, v160
	v_cvt_pk_fp8_f32 v148, v158, v159 op_sel:[0,0,1]
	v_mul_f32_e32 v156, 0x44000000, v100
	v_mul_f32_e32 v157, 0x44000000, v104
	v_med3_f32 v156, v156, s35, v160
	v_med3_f32 v157, v157, s35, v160
	v_cvt_pk_fp8_f32 v149, v156, v157
	v_mul_f32_e32 v158, 0x44000000, v108
	v_mul_f32_e32 v159, 0x44000000, v112
	v_med3_f32 v158, v158, s35, v160
	v_med3_f32 v159, v159, s35, v160
	v_cvt_pk_fp8_f32 v149, v158, v159 op_sel:[0,0,1]
	v_mul_f32_e32 v156, 0x44000000, v85
	v_mul_f32_e32 v157, 0x44000000, v89
	v_med3_f32 v156, v156, s35, v160
	v_med3_f32 v157, v157, s35, v160
	v_cvt_pk_fp8_f32 v150, v156, v157
	v_mul_f32_e32 v158, 0x44000000, v93
	v_mul_f32_e32 v159, 0x44000000, v97
	v_med3_f32 v158, v158, s35, v160
	v_med3_f32 v159, v159, s35, v160
	v_cvt_pk_fp8_f32 v150, v158, v159 op_sel:[0,0,1]
	v_mul_f32_e32 v156, 0x44000000, v101
	v_mul_f32_e32 v157, 0x44000000, v105
	v_med3_f32 v156, v156, s35, v160
	v_med3_f32 v157, v157, s35, v160
	v_cvt_pk_fp8_f32 v151, v156, v157
	v_mul_f32_e32 v158, 0x44000000, v109
	v_mul_f32_e32 v159, 0x44000000, v113
	v_med3_f32 v158, v158, s35, v160
	v_med3_f32 v159, v159, s35, v160
	v_cvt_pk_fp8_f32 v151, v158, v159 op_sel:[0,0,1]
	v_mul_f32_e32 v156, 0x44000000, v86
	v_mul_f32_e32 v157, 0x44000000, v90
	v_med3_f32 v156, v156, s35, v160
	v_med3_f32 v157, v157, s35, v160
	v_cvt_pk_fp8_f32 v152, v156, v157
	v_mul_f32_e32 v158, 0x44000000, v94
	v_mul_f32_e32 v159, 0x44000000, v98
	v_med3_f32 v158, v158, s35, v160
	v_med3_f32 v159, v159, s35, v160
	v_cvt_pk_fp8_f32 v152, v158, v159 op_sel:[0,0,1]
	ds_write2_b64 v73, v[148:149], v[150:151] offset0:0 offset1:16
	v_mul_f32_e32 v156, 0x44000000, v102
	v_mul_f32_e32 v157, 0x44000000, v106
	v_med3_f32 v156, v156, s35, v160
	v_med3_f32 v157, v157, s35, v160
	v_cvt_pk_fp8_f32 v153, v156, v157
	v_mul_f32_e32 v158, 0x44000000, v110
	v_mul_f32_e32 v159, 0x44000000, v114
	v_med3_f32 v158, v158, s35, v160
	v_med3_f32 v159, v159, s35, v160
	v_cvt_pk_fp8_f32 v153, v158, v159 op_sel:[0,0,1]
	v_mul_f32_e32 v156, 0x44000000, v87
	v_mul_f32_e32 v157, 0x44000000, v91
	v_med3_f32 v156, v156, s35, v160
	v_med3_f32 v157, v157, s35, v160
	v_cvt_pk_fp8_f32 v154, v156, v157
	v_mul_f32_e32 v158, 0x44000000, v95
	v_mul_f32_e32 v159, 0x44000000, v99
	v_med3_f32 v158, v158, s35, v160
	v_med3_f32 v159, v159, s35, v160
	v_cvt_pk_fp8_f32 v154, v158, v159 op_sel:[0,0,1]
	v_mul_f32_e32 v156, 0x44000000, v103
	v_mul_f32_e32 v157, 0x44000000, v107
	v_med3_f32 v156, v156, s35, v160
	v_med3_f32 v157, v157, s35, v160
	v_cvt_pk_fp8_f32 v155, v156, v157
	v_mul_f32_e32 v158, 0x44000000, v111
	v_mul_f32_e32 v159, 0x44000000, v115
	v_med3_f32 v158, v158, s35, v160
	v_med3_f32 v159, v159, s35, v160
	v_cvt_pk_fp8_f32 v155, v158, v159 op_sel:[0,0,1]
	v_mul_f32_e32 v156, 0x44000000, v116
	v_mul_f32_e32 v157, 0x44000000, v120
	v_med3_f32 v156, v156, s35, v160
	v_med3_f32 v157, v157, s35, v160
	v_cvt_pk_fp8_f32 v148, v156, v157
	v_mul_f32_e32 v158, 0x44000000, v124
	v_mul_f32_e32 v159, 0x44000000, v128
	v_med3_f32 v158, v158, s35, v160
	v_med3_f32 v159, v159, s35, v160
	v_cvt_pk_fp8_f32 v148, v158, v159 op_sel:[0,0,1]
	ds_write2_b64 v73, v[152:153], v[154:155] offset0:32 offset1:48
	v_mul_f32_e32 v156, 0x44000000, v132
	v_mul_f32_e32 v157, 0x44000000, v136
	v_med3_f32 v156, v156, s35, v160
	v_med3_f32 v157, v157, s35, v160
	v_cvt_pk_fp8_f32 v149, v156, v157
	v_mul_f32_e32 v158, 0x44000000, v140
	v_mul_f32_e32 v159, 0x44000000, v144
	v_med3_f32 v158, v158, s35, v160
	v_med3_f32 v159, v159, s35, v160
	v_cvt_pk_fp8_f32 v149, v158, v159 op_sel:[0,0,1]
	v_mul_f32_e32 v156, 0x44000000, v117
	v_mul_f32_e32 v157, 0x44000000, v121
	v_med3_f32 v156, v156, s35, v160
	v_med3_f32 v157, v157, s35, v160
	v_cvt_pk_fp8_f32 v150, v156, v157
	v_mul_f32_e32 v158, 0x44000000, v125
	v_mul_f32_e32 v159, 0x44000000, v129
	v_med3_f32 v158, v158, s35, v160
	v_med3_f32 v159, v159, s35, v160
	v_cvt_pk_fp8_f32 v150, v158, v159 op_sel:[0,0,1]
	v_mul_f32_e32 v156, 0x44000000, v133
	v_mul_f32_e32 v157, 0x44000000, v137
	v_med3_f32 v156, v156, s35, v160
	v_med3_f32 v157, v157, s35, v160
	v_cvt_pk_fp8_f32 v151, v156, v157
	v_mul_f32_e32 v158, 0x44000000, v141
	v_mul_f32_e32 v159, 0x44000000, v145
	v_med3_f32 v158, v158, s35, v160
	v_med3_f32 v159, v159, s35, v160
	v_cvt_pk_fp8_f32 v151, v158, v159 op_sel:[0,0,1]
	v_mul_f32_e32 v156, 0x44000000, v118
	v_mul_f32_e32 v157, 0x44000000, v122
	v_med3_f32 v156, v156, s35, v160
	v_med3_f32 v157, v157, s35, v160
	v_cvt_pk_fp8_f32 v152, v156, v157
	v_mul_f32_e32 v158, 0x44000000, v126
	v_mul_f32_e32 v159, 0x44000000, v130
	v_med3_f32 v158, v158, s35, v160
	v_med3_f32 v159, v159, s35, v160
	v_cvt_pk_fp8_f32 v152, v158, v159 op_sel:[0,0,1]
	ds_write2_b64 v74, v[148:149], v[150:151] offset0:0 offset1:16
	v_mul_f32_e32 v156, 0x44000000, v134
	v_mul_f32_e32 v157, 0x44000000, v138
	v_med3_f32 v156, v156, s35, v160
	v_med3_f32 v157, v157, s35, v160
	v_cvt_pk_fp8_f32 v153, v156, v157
	v_mul_f32_e32 v158, 0x44000000, v142
	v_mul_f32_e32 v159, 0x44000000, v146
	v_med3_f32 v158, v158, s35, v160
	v_med3_f32 v159, v159, s35, v160
	v_cvt_pk_fp8_f32 v153, v158, v159 op_sel:[0,0,1]
	v_mul_f32_e32 v156, 0x44000000, v119
	v_mul_f32_e32 v157, 0x44000000, v123
	v_med3_f32 v156, v156, s35, v160
	v_med3_f32 v157, v157, s35, v160
	v_cvt_pk_fp8_f32 v154, v156, v157
	v_mul_f32_e32 v158, 0x44000000, v127
	v_mul_f32_e32 v159, 0x44000000, v131
	v_med3_f32 v158, v158, s35, v160
	v_med3_f32 v159, v159, s35, v160
	v_cvt_pk_fp8_f32 v154, v158, v159 op_sel:[0,0,1]
	v_mul_f32_e32 v156, 0x44000000, v135
	v_mul_f32_e32 v157, 0x44000000, v139
	v_med3_f32 v156, v156, s35, v160
	v_med3_f32 v157, v157, s35, v160
	v_cvt_pk_fp8_f32 v155, v156, v157
	v_mul_f32_e32 v158, 0x44000000, v143
	v_mul_f32_e32 v159, 0x44000000, v147
	v_med3_f32 v158, v158, s35, v160
	v_med3_f32 v159, v159, s35, v160
	v_cvt_pk_fp8_f32 v155, v158, v159 op_sel:[0,0,1]
	s_nop 0
	ds_write2_b64 v74, v[152:153], v[154:155] offset0:32 offset1:48
	s_waitcnt lgkmcnt(0)
	s_barrier
	ds_read_b128 v[236:239], v75 offset:32768
	ds_read_b128 v[240:243], v75 offset:40960
	ds_read_b128 v[244:247], v75 offset:49152
	ds_read_b128 v[248:251], v75 offset:57344
	s_mov_b64 s[68:69], s[58:59]
	s_waitcnt lgkmcnt(3)
	global_store_dwordx4 v76, v[236:239], s[68:69] nt
	s_add_u32 s68, s68, 0x20000
	s_addc_u32 s69, s69, 0
	s_waitcnt lgkmcnt(2)
	global_store_dwordx4 v76, v[240:243], s[68:69] nt
	s_add_u32 s68, s68, s87
	s_addc_u32 s69, s69, 0
	s_waitcnt lgkmcnt(1)
	global_store_dwordx4 v76, v[244:247], s[68:69] nt
	s_add_u32 s68, s68, 0x20000
	s_addc_u32 s69, s69, 0
	s_waitcnt lgkmcnt(0)
	global_store_dwordx4 v76, v[248:251], s[68:69] nt
	s_sub_u32 s41, s41, 1
	s_cmp_eq_u32 s41, 0
	s_cbranch_scc1 .Lcv_done
	s_min_u32 s0, s30, 0x2fff
	s_add_u32 s30, s30, s31
	s_cmp_lt_u32 s0, 0x2000
	s_cbranch_scc0 .Lcv_w2_4
	s_lshr_b32 s1, s0, 8
	s_bfe_u32 s3, s0, 0x40004
	s_bfe_u32 s7, s0, 0x30001
	s_and_b32 s0, s0, 1
	s_lshl_b32 s6, s1, 25
	s_lshl_b32 s49, s3, 21
	s_add_u32 s6, s6, s49
	s_lshl_b32 s49, s34, 17
	s_add_u32 s6, s6, s49
	s_lshl_b32 s49, s0, 13
	s_add_u32 s6, s6, s49
	s_lshl_b32 s49, s7, 10
	s_add_u32 s6, s6, s49
	s_add_u32 s62, s8, s6
	s_addc_u32 s63, s9, 0
	s_lshl_b32 s6, s1, 23
	s_lshl_b32 s49, s7, 20
	s_add_u32 s6, s6, s49
	s_lshl_b32 s49, s0, 18
	s_add_u32 s6, s6, s49
	s_lshl_b32 s49, s3, 7
	s_add_u32 s6, s6, s49
	s_add_u32 s58, s12, s6
	s_addc_u32 s59, s13, 0
	s_mov_b32 s70, 0x4000
	s_mov_b32 s71, 0xe4000
	s_mov_b32 s87, 0x60000
	v_mov_b32_e32 v70, v68
	s_branch .Lcv_dec_done_4
